# stack + odd-half A-tile DMA offsets/addresses formed in the even half's MFMA segment (four LDS-DMA loads issue right after the barrier)
# baseline (speedup 1.0000x reference)
.LBB0_726:
	s_cmp_lg_u64 s[2:3], 0
	s_cbranch_scc1 .Lswp_guE_half
	ds_read_b64_tr_b16 v[162:163], v190 offset:0
	ds_read_b64_tr_b16 v[164:165], v191 offset:0
	ds_read_b64_tr_b16 v[170:171], v192 offset:0
	ds_read_b64_tr_b16 v[172:173], v193 offset:0
	ds_read_b128 v[214:217], v207
	ds_read_b128 v[224:227], v207 offset:2048
	ds_read_b128 v[232:235], v207 offset:4096
	ds_read_b128 v[240:243], v207 offset:6144
	ds_read_b64_tr_b16 v[166:167], v190 offset:8192
	ds_read_b64_tr_b16 v[168:169], v191 offset:8192
	ds_read_b64_tr_b16 v[174:175], v192 offset:8192
	ds_read_b64_tr_b16 v[176:177], v193 offset:8192
	ds_read_b128 v[218:221], v207 offset:1024
	ds_read_b128 v[228:231], v207 offset:3072
	ds_read_b128 v[236:239], v207 offset:5120
	ds_read_b128 v[244:247], v207 offset:7168
	s_add_i32 s38, s4, 2
	s_cmp_eq_u32 s34, 28
	s_cselect_b64 s[4:5], -1, 0
	s_and_b64 s[34:35], s[4:5], exec
	s_cselect_b32 s38, 0, s38
	s_cselect_b32 s34, s23, s37
	s_cselect_b32 s35, s22, s36
	s_cselect_b32 s66, s21, s25
	s_cselect_b32 s67, s20, s24
	s_ashr_i32 s39, s38, 31
	s_lshl_b64 s[40:41], s[38:39], 18
	s_add_u32 s68, s67, s40
	s_addc_u32 s69, s66, s41
	s_add_u32 s40, s35, s40
	s_addc_u32 s41, s34, s41
	v_cndmask_b32_e64 v250, v178, v209, s[4:5]
	v_cndmask_b32_e64 v251, v180, v210, s[4:5]
	v_cndmask_b32_e64 v252, v182, v211, s[4:5]
	v_cndmask_b32_e64 v253, v184, v212, s[4:5]
	v_cndmask_b32_e64 v222, v213, v208, s[4:5]
	s_setprio 1
	s_waitcnt lgkmcnt(11)
	v_mfma_f32_16x16x32_bf16 v[158:161], v[162:165], v[214:217], v[158:161]
	v_mfma_f32_16x16x32_bf16 v[154:157], v[170:173], v[214:217], v[154:157]
	s_waitcnt lgkmcnt(10)
	v_mfma_f32_16x16x32_bf16 v[146:149], v[162:165], v[224:227], v[146:149]
	v_mfma_f32_16x16x32_bf16 v[138:141], v[170:173], v[224:227], v[138:141]
	s_waitcnt lgkmcnt(9)
	v_mfma_f32_16x16x32_bf16 v[130:133], v[162:165], v[232:235], v[130:133]
	v_mfma_f32_16x16x32_bf16 v[122:125], v[170:173], v[232:235], v[122:125]
	s_waitcnt lgkmcnt(8)
	v_mfma_f32_16x16x32_bf16 v[114:117], v[162:165], v[240:243], v[114:117]
	v_mfma_f32_16x16x32_bf16 v[106:109], v[170:173], v[240:243], v[106:109]
	ds_read_b64_tr_b16 v[162:163], v190 offset:16384
	ds_read_b64_tr_b16 v[164:165], v191 offset:16384
	ds_read_b64_tr_b16 v[170:171], v192 offset:16384
	ds_read_b64_tr_b16 v[172:173], v193 offset:16384
	s_waitcnt lgkmcnt(7)
	v_mfma_f32_16x16x32_bf16 v[158:161], v[166:169], v[218:221], v[158:161]
	v_mfma_f32_16x16x32_bf16 v[154:157], v[174:177], v[218:221], v[154:157]
	s_waitcnt lgkmcnt(6)
	v_mfma_f32_16x16x32_bf16 v[146:149], v[166:169], v[228:231], v[146:149]
	v_mfma_f32_16x16x32_bf16 v[138:141], v[174:177], v[228:231], v[138:141]
	s_waitcnt lgkmcnt(5)
	v_mfma_f32_16x16x32_bf16 v[130:133], v[166:169], v[236:239], v[130:133]
	v_mfma_f32_16x16x32_bf16 v[122:125], v[174:177], v[236:239], v[122:125]
	s_waitcnt lgkmcnt(4)
	v_mfma_f32_16x16x32_bf16 v[114:117], v[166:169], v[244:247], v[114:117]
	v_mfma_f32_16x16x32_bf16 v[106:109], v[174:177], v[244:247], v[106:109]
	ds_read_b64_tr_b16 v[166:167], v190 offset:24576
	ds_read_b64_tr_b16 v[168:169], v191 offset:24576
	ds_read_b64_tr_b16 v[174:175], v192 offset:24576
	ds_read_b64_tr_b16 v[176:177], v193 offset:24576
	s_waitcnt lgkmcnt(4)
	v_mfma_f32_16x16x32_bf16 v[150:153], v[162:165], v[214:217], v[150:153]
	v_mfma_f32_16x16x32_bf16 v[142:145], v[170:173], v[214:217], v[142:145]
	ds_read_b128 v[214:217], v207 offset:16384
	v_mfma_f32_16x16x32_bf16 v[134:137], v[162:165], v[224:227], v[134:137]
	v_mfma_f32_16x16x32_bf16 v[126:129], v[170:173], v[224:227], v[126:129]
	ds_read_b128 v[224:227], v207 offset:18432
	v_mfma_f32_16x16x32_bf16 v[118:121], v[162:165], v[232:235], v[118:121]
	v_mfma_f32_16x16x32_bf16 v[110:113], v[170:173], v[232:235], v[110:113]
	ds_read_b128 v[232:235], v207 offset:20480
	v_mfma_f32_16x16x32_bf16 v[102:105], v[162:165], v[240:243], v[102:105]
	v_mfma_f32_16x16x32_bf16 v[98:101], v[170:173], v[240:243], v[98:101]
	ds_read_b128 v[240:243], v207 offset:22528
	ds_read_b64_tr_b16 v[162:163], v190 offset:0
	ds_read_b64_tr_b16 v[164:165], v191 offset:0
	ds_read_b64_tr_b16 v[170:171], v192 offset:0
	ds_read_b64_tr_b16 v[172:173], v193 offset:0
	s_waitcnt lgkmcnt(8)
	v_mfma_f32_16x16x32_bf16 v[150:153], v[166:169], v[218:221], v[150:153]
	v_mfma_f32_16x16x32_bf16 v[142:145], v[174:177], v[218:221], v[142:145]
	ds_read_b128 v[218:221], v207 offset:17408
	v_mfma_f32_16x16x32_bf16 v[134:137], v[166:169], v[228:231], v[134:137]
	v_mfma_f32_16x16x32_bf16 v[126:129], v[174:177], v[228:231], v[126:129]
	ds_read_b128 v[228:231], v207 offset:19456
	v_mfma_f32_16x16x32_bf16 v[118:121], v[166:169], v[236:239], v[118:121]
	v_mfma_f32_16x16x32_bf16 v[110:113], v[174:177], v[236:239], v[110:113]
	ds_read_b128 v[236:239], v207 offset:21504
	v_mfma_f32_16x16x32_bf16 v[102:105], v[166:169], v[244:247], v[102:105]
	v_mfma_f32_16x16x32_bf16 v[98:101], v[174:177], v[244:247], v[98:101]
	ds_read_b128 v[244:247], v207 offset:23552
	ds_read_b64_tr_b16 v[166:167], v190 offset:8192
	ds_read_b64_tr_b16 v[168:169], v191 offset:8192
	ds_read_b64_tr_b16 v[174:175], v192 offset:8192
	ds_read_b64_tr_b16 v[176:177], v193 offset:8192
	s_waitcnt lgkmcnt(8)
	v_mfma_f32_16x16x32_bf16 v[94:97], v[162:165], v[214:217], v[94:97]
	v_mfma_f32_16x16x32_bf16 v[86:89], v[170:173], v[214:217], v[86:89]
	v_mfma_f32_16x16x32_bf16 v[78:81], v[162:165], v[224:227], v[78:81]
	v_mfma_f32_16x16x32_bf16 v[70:73], v[170:173], v[224:227], v[70:73]
	v_mfma_f32_16x16x32_bf16 v[62:65], v[162:165], v[232:235], v[62:65]
	v_mfma_f32_16x16x32_bf16 v[54:57], v[170:173], v[232:235], v[54:57]
	v_mfma_f32_16x16x32_bf16 v[46:49], v[162:165], v[240:243], v[46:49]
	v_mfma_f32_16x16x32_bf16 v[38:41], v[170:173], v[240:243], v[38:41]
	ds_read_b64_tr_b16 v[162:163], v190 offset:16384
	ds_read_b64_tr_b16 v[164:165], v191 offset:16384
	ds_read_b64_tr_b16 v[170:171], v192 offset:16384
	ds_read_b64_tr_b16 v[172:173], v193 offset:16384
	s_waitcnt lgkmcnt(4)
	v_mfma_f32_16x16x32_bf16 v[94:97], v[166:169], v[218:221], v[94:97]
	v_mfma_f32_16x16x32_bf16 v[86:89], v[174:177], v[218:221], v[86:89]
	v_mfma_f32_16x16x32_bf16 v[78:81], v[166:169], v[228:231], v[78:81]
	v_mfma_f32_16x16x32_bf16 v[70:73], v[174:177], v[228:231], v[70:73]
	v_mfma_f32_16x16x32_bf16 v[62:65], v[166:169], v[236:239], v[62:65]
	v_mfma_f32_16x16x32_bf16 v[54:57], v[174:177], v[236:239], v[54:57]
	v_mfma_f32_16x16x32_bf16 v[46:49], v[166:169], v[244:247], v[46:49]
	v_mfma_f32_16x16x32_bf16 v[38:41], v[174:177], v[244:247], v[38:41]
	ds_read_b64_tr_b16 v[166:167], v190 offset:24576
	ds_read_b64_tr_b16 v[168:169], v191 offset:24576
	ds_read_b64_tr_b16 v[174:175], v192 offset:24576
	ds_read_b64_tr_b16 v[176:177], v193 offset:24576
	s_waitcnt lgkmcnt(4)
	v_mfma_f32_16x16x32_bf16 v[90:93], v[162:165], v[214:217], v[90:93]
	v_mfma_f32_16x16x32_bf16 v[82:85], v[170:173], v[214:217], v[82:85]
	s_waitcnt vmcnt(11)
	v_cvt_pk_bf16_f32 v248, v2, v3
	v_cvt_pk_bf16_f32 v249, v4, v5
	ds_write_b64 v199, v[248:249]
	s_add_u32 s70, s40, 0x6000
	s_addc_u32 s71, s41, 0
	global_load_dwordx4 v[2:5], v189, s[70:71]
	v_mfma_f32_16x16x32_bf16 v[74:77], v[162:165], v[224:227], v[74:77]
	v_mfma_f32_16x16x32_bf16 v[66:69], v[170:173], v[224:227], v[66:69]
	s_waitcnt vmcnt(11)
	v_cvt_pk_bf16_f32 v248, v6, v7
	v_cvt_pk_bf16_f32 v249, v8, v9
	ds_write_b64 v200, v[248:249]
	s_add_u32 s72, s40, 0x4000
	s_addc_u32 s73, s41, 0
	global_load_dwordx4 v[6:9], v189, s[72:73]
	v_mfma_f32_16x16x32_bf16 v[58:61], v[162:165], v[232:235], v[58:61]
	v_mfma_f32_16x16x32_bf16 v[50:53], v[170:173], v[232:235], v[50:53]
	s_waitcnt vmcnt(11)
	v_cvt_pk_bf16_f32 v248, v10, v11
	v_cvt_pk_bf16_f32 v249, v12, v13
	ds_write_b64 v201, v[248:249]
	s_add_u32 s70, s68, 0x6000
	s_addc_u32 s71, s69, 0
	global_load_dwordx4 v[10:13], v189, s[70:71]
	v_mfma_f32_16x16x32_bf16 v[42:45], v[162:165], v[240:243], v[42:45]
	v_mfma_f32_16x16x32_bf16 v[30:33], v[170:173], v[240:243], v[30:33]
	s_waitcnt vmcnt(11)
	v_cvt_pk_bf16_f32 v248, v14, v15
	v_cvt_pk_bf16_f32 v249, v16, v17
	ds_write_b64 v202, v[248:249]
	s_add_u32 s72, s40, 0x2000
	s_addc_u32 s73, s41, 0
	global_load_dwordx4 v[14:17], v189, s[72:73]
	s_waitcnt lgkmcnt(4)
	v_mfma_f32_16x16x32_bf16 v[90:93], v[166:169], v[218:221], v[90:93]
	v_mfma_f32_16x16x32_bf16 v[82:85], v[174:177], v[218:221], v[82:85]
	s_waitcnt vmcnt(11)
	v_cvt_pk_bf16_f32 v248, v18, v19
	v_cvt_pk_bf16_f32 v249, v20, v21
	ds_write_b64 v203, v[248:249]
	s_add_u32 s70, s68, 0x4000
	s_addc_u32 s71, s69, 0
	global_load_dwordx4 v[18:21], v189, s[70:71]
	v_mfma_f32_16x16x32_bf16 v[74:77], v[166:169], v[228:231], v[74:77]
	v_mfma_f32_16x16x32_bf16 v[66:69], v[174:177], v[228:231], v[66:69]
	s_waitcnt vmcnt(11)
	v_cvt_pk_bf16_f32 v248, v22, v23
	v_cvt_pk_bf16_f32 v249, v24, v25
	ds_write_b64 v204, v[248:249]
	global_load_dwordx4 v[22:25], v189, s[40:41]
	v_mfma_f32_16x16x32_bf16 v[58:61], v[166:169], v[236:239], v[58:61]
	v_mfma_f32_16x16x32_bf16 v[50:53], v[174:177], v[236:239], v[50:53]
	s_waitcnt vmcnt(11)
	v_cvt_pk_bf16_f32 v248, v26, v27
	v_cvt_pk_bf16_f32 v249, v28, v29
	ds_write_b64 v205, v[248:249]
	s_add_u32 s70, s68, 0x2000
	s_addc_u32 s71, s69, 0
	global_load_dwordx4 v[26:29], v189, s[70:71]
	v_mfma_f32_16x16x32_bf16 v[42:45], v[166:169], v[244:247], v[42:45]
	v_mfma_f32_16x16x32_bf16 v[30:33], v[174:177], v[244:247], v[30:33]
	s_waitcnt vmcnt(11)
	v_cvt_pk_bf16_f32 v248, v34, v35
	v_cvt_pk_bf16_f32 v249, v36, v37
	ds_write_b64 v206, v[248:249]
	global_load_dwordx4 v[34:37], v189, s[68:69]
	s_setprio 0
.LBB0_730:
.Lswp_guE_tail:
	s_lshl_b64 s[40:41], s[38:39], 7
	s_add_u32 s40, s8, s40
	s_addc_u32 s41, s9, s41
	s_mov_b32 m0, s51
	s_waitcnt vmcnt(8)
	s_waitcnt lgkmcnt(0)
	s_barrier
	global_load_lds_dwordx4 v250, s[40:41]
	s_mov_b32 m0, s60
	v_cmp_ne_u32_e32 vcc, 0, v222
	global_load_lds_dwordx4 v251, s[40:41]
	s_mov_b64 s[96:97], vcc
	s_add_i32 m0, s51, 0x4000
	s_cbranch_vccnz .LBB0_732
	global_load_lds_dwordx4 v252, s[40:41]
	s_add_i32 m0, s51, 0x6000
	s_nop 0
	global_load_lds_dwordx4 v253, s[40:41]

.Lswp_guE_half:
	ds_read_b64_tr_b16 v[162:163], v190 offset:0
	ds_read_b64_tr_b16 v[164:165], v191 offset:0
	ds_read_b64_tr_b16 v[170:171], v192 offset:0
	ds_read_b64_tr_b16 v[172:173], v193 offset:0
	ds_read_b128 v[214:217], v207
	ds_read_b128 v[224:227], v207 offset:2048
	ds_read_b128 v[232:235], v207 offset:4096
	ds_read_b128 v[240:243], v207 offset:6144
	ds_read_b64_tr_b16 v[166:167], v190 offset:8192
	ds_read_b64_tr_b16 v[168:169], v191 offset:8192
	ds_read_b64_tr_b16 v[174:175], v192 offset:8192
	ds_read_b64_tr_b16 v[176:177], v193 offset:8192
	ds_read_b128 v[218:221], v207 offset:1024
	ds_read_b128 v[228:231], v207 offset:3072
	ds_read_b128 v[236:239], v207 offset:5120
	ds_read_b128 v[244:247], v207 offset:7168
	s_add_i32 s38, s4, 2
	s_cmp_eq_u32 s34, 28
	s_cselect_b64 s[4:5], -1, 0
	s_and_b64 s[34:35], s[4:5], exec
	s_cselect_b32 s38, 0, s38
	s_cselect_b32 s34, s23, s37
	s_cselect_b32 s35, s22, s36
	s_cselect_b32 s66, s21, s25
	s_cselect_b32 s67, s20, s24
	s_ashr_i32 s39, s38, 31
	s_lshl_b64 s[40:41], s[38:39], 18
	s_add_u32 s68, s67, s40
	s_addc_u32 s69, s66, s41
	s_add_u32 s40, s35, s40
	s_addc_u32 s41, s34, s41
	v_cndmask_b32_e64 v250, v178, v209, s[4:5]
	v_cndmask_b32_e64 v251, v180, v210, s[4:5]
	v_cndmask_b32_e64 v252, v182, v211, s[4:5]
	v_cndmask_b32_e64 v253, v184, v212, s[4:5]
	v_cndmask_b32_e64 v222, v213, v208, s[4:5]
	s_setprio 1
	s_waitcnt lgkmcnt(11)
	v_mfma_f32_16x16x32_bf16 v[158:161], v[162:165], v[214:217], v[158:161]
	v_mfma_f32_16x16x32_bf16 v[154:157], v[170:173], v[214:217], v[154:157]
	s_waitcnt lgkmcnt(10)
	v_mfma_f32_16x16x32_bf16 v[146:149], v[162:165], v[224:227], v[146:149]
	v_mfma_f32_16x16x32_bf16 v[138:141], v[170:173], v[224:227], v[138:141]
	s_waitcnt lgkmcnt(9)
	v_mfma_f32_16x16x32_bf16 v[130:133], v[162:165], v[232:235], v[130:133]
	v_mfma_f32_16x16x32_bf16 v[122:125], v[170:173], v[232:235], v[122:125]
	s_waitcnt lgkmcnt(8)
	v_mfma_f32_16x16x32_bf16 v[114:117], v[162:165], v[240:243], v[114:117]
	v_mfma_f32_16x16x32_bf16 v[106:109], v[170:173], v[240:243], v[106:109]
	ds_read_b64_tr_b16 v[162:163], v190 offset:16384
	ds_read_b64_tr_b16 v[164:165], v191 offset:16384
	ds_read_b64_tr_b16 v[170:171], v192 offset:16384
	ds_read_b64_tr_b16 v[172:173], v193 offset:16384
	s_waitcnt lgkmcnt(7)
	v_mfma_f32_16x16x32_bf16 v[158:161], v[166:169], v[218:221], v[158:161]
	v_mfma_f32_16x16x32_bf16 v[154:157], v[174:177], v[218:221], v[154:157]
	s_waitcnt lgkmcnt(6)
	v_mfma_f32_16x16x32_bf16 v[146:149], v[166:169], v[228:231], v[146:149]
	v_mfma_f32_16x16x32_bf16 v[138:141], v[174:177], v[228:231], v[138:141]
	s_waitcnt lgkmcnt(5)
	v_mfma_f32_16x16x32_bf16 v[130:133], v[166:169], v[236:239], v[130:133]
	v_mfma_f32_16x16x32_bf16 v[122:125], v[174:177], v[236:239], v[122:125]
	s_waitcnt lgkmcnt(4)
	v_mfma_f32_16x16x32_bf16 v[114:117], v[166:169], v[244:247], v[114:117]
	v_mfma_f32_16x16x32_bf16 v[106:109], v[174:177], v[244:247], v[106:109]
	ds_read_b64_tr_b16 v[166:167], v190 offset:24576
	ds_read_b64_tr_b16 v[168:169], v191 offset:24576
	ds_read_b64_tr_b16 v[174:175], v192 offset:24576
	ds_read_b64_tr_b16 v[176:177], v193 offset:24576
	s_waitcnt lgkmcnt(4)
	v_mfma_f32_16x16x32_bf16 v[150:153], v[162:165], v[214:217], v[150:153]
	v_mfma_f32_16x16x32_bf16 v[142:145], v[170:173], v[214:217], v[142:145]
	s_waitcnt vmcnt(9)
	v_cvt_pk_bf16_f32 v248, v2, v3
	v_cvt_pk_bf16_f32 v249, v4, v5
	ds_write_b64 v199, v[248:249]
	s_add_u32 s70, s40, 0x6000
	s_addc_u32 s71, s41, 0
	global_load_dwordx4 v[2:5], v189, s[70:71]
	v_mfma_f32_16x16x32_bf16 v[134:137], v[162:165], v[224:227], v[134:137]
	v_mfma_f32_16x16x32_bf16 v[126:129], v[170:173], v[224:227], v[126:129]
	s_waitcnt vmcnt(9)
	v_cvt_pk_bf16_f32 v248, v6, v7
	v_cvt_pk_bf16_f32 v249, v8, v9
	ds_write_b64 v200, v[248:249]
	s_add_u32 s72, s40, 0x4000
	s_addc_u32 s73, s41, 0
	global_load_dwordx4 v[6:9], v189, s[72:73]
	v_mfma_f32_16x16x32_bf16 v[118:121], v[162:165], v[232:235], v[118:121]
	v_mfma_f32_16x16x32_bf16 v[110:113], v[170:173], v[232:235], v[110:113]
	s_waitcnt vmcnt(9)
	v_cvt_pk_bf16_f32 v248, v10, v11
	v_cvt_pk_bf16_f32 v249, v12, v13
	ds_write_b64 v201, v[248:249]
	s_add_u32 s70, s68, 0x6000
	s_addc_u32 s71, s69, 0
	global_load_dwordx4 v[10:13], v189, s[70:71]
	v_mfma_f32_16x16x32_bf16 v[102:105], v[162:165], v[240:243], v[102:105]
	v_mfma_f32_16x16x32_bf16 v[98:101], v[170:173], v[240:243], v[98:101]
	s_waitcnt vmcnt(9)
	v_cvt_pk_bf16_f32 v248, v14, v15
	v_cvt_pk_bf16_f32 v249, v16, v17
	ds_write_b64 v202, v[248:249]
	s_add_u32 s72, s40, 0x2000
	s_addc_u32 s73, s41, 0
	global_load_dwordx4 v[14:17], v189, s[72:73]
	s_waitcnt lgkmcnt(4)
	v_mfma_f32_16x16x32_bf16 v[150:153], v[166:169], v[218:221], v[150:153]
	v_mfma_f32_16x16x32_bf16 v[142:145], v[174:177], v[218:221], v[142:145]
	s_waitcnt vmcnt(9)
	v_cvt_pk_bf16_f32 v248, v18, v19
	v_cvt_pk_bf16_f32 v249, v20, v21
	ds_write_b64 v203, v[248:249]
	s_add_u32 s70, s68, 0x4000
	s_addc_u32 s71, s69, 0
	global_load_dwordx4 v[18:21], v189, s[70:71]
	v_mfma_f32_16x16x32_bf16 v[134:137], v[166:169], v[228:231], v[134:137]
	v_mfma_f32_16x16x32_bf16 v[126:129], v[174:177], v[228:231], v[126:129]
	s_waitcnt vmcnt(9)
	v_cvt_pk_bf16_f32 v248, v22, v23
	v_cvt_pk_bf16_f32 v249, v24, v25
	ds_write_b64 v204, v[248:249]
	global_load_dwordx4 v[22:25], v189, s[40:41]
	v_mfma_f32_16x16x32_bf16 v[118:121], v[166:169], v[236:239], v[118:121]
	v_mfma_f32_16x16x32_bf16 v[110:113], v[174:177], v[236:239], v[110:113]
	s_waitcnt vmcnt(9)
	v_cvt_pk_bf16_f32 v248, v26, v27
	v_cvt_pk_bf16_f32 v249, v28, v29
	ds_write_b64 v205, v[248:249]
	s_add_u32 s70, s68, 0x2000
	s_addc_u32 s71, s69, 0
	global_load_dwordx4 v[26:29], v189, s[70:71]
	v_mfma_f32_16x16x32_bf16 v[102:105], v[166:169], v[244:247], v[102:105]
	v_mfma_f32_16x16x32_bf16 v[98:101], v[174:177], v[244:247], v[98:101]
	s_waitcnt vmcnt(9)
	v_cvt_pk_bf16_f32 v248, v34, v35
	v_cvt_pk_bf16_f32 v249, v36, v37
	ds_write_b64 v206, v[248:249]
	global_load_dwordx4 v[34:37], v189, s[68:69]
	s_setprio 0
	s_branch .Lswp_guE_tail

.LBB0_858:
	s_cmp_lg_u64 s[2:3], 0
	s_cbranch_scc1 .Lswp_dnE_half
	ds_read_b64_tr_b16 v[164:165], v190 offset:0
	ds_read_b64_tr_b16 v[166:167], v191 offset:0
	ds_read_b64_tr_b16 v[172:173], v192 offset:0
	ds_read_b64_tr_b16 v[174:175], v193 offset:0
	ds_read_b128 v[210:213], v207
	ds_read_b128 v[218:221], v207 offset:2048
	ds_read_b128 v[228:231], v207 offset:4096
	ds_read_b128 v[236:239], v207 offset:6144
	ds_read_b64_tr_b16 v[168:169], v190 offset:8192
	ds_read_b64_tr_b16 v[170:171], v191 offset:8192
	ds_read_b64_tr_b16 v[176:177], v192 offset:8192
	ds_read_b64_tr_b16 v[178:179], v193 offset:8192
	ds_read_b128 v[214:217], v207 offset:1024
	ds_read_b128 v[224:227], v207 offset:3072
	ds_read_b128 v[232:235], v207 offset:5120
	ds_read_b128 v[240:243], v207 offset:7168
	s_add_i32 s48, s48, 2
	s_cmp_eq_u32 s35, 12
	s_cselect_b32 s48, 0, s48
	s_cselect_b32 s77, s41, s23
	s_cselect_b32 s82, s40, s22
	s_cselect_b32 s35, s39, s47
	s_cselect_b32 s37, s38, s46
	s_cselect_b32 s43, s27, s45
	s_cselect_b32 s74, s26, s44
	s_cselect_b64 vcc, -1, 0
	s_ashr_i32 s49, s48, 31
	s_lshl_b64 s[50:51], s[48:49], 19
	s_add_u32 s72, s74, s50
	s_addc_u32 s73, s43, s51
	s_add_u32 s50, s37, s50
	s_addc_u32 s51, s35, s51
	s_lshl_b64 s[92:93], s[48:49], 7
	s_add_u32 s92, s82, s92
	s_addc_u32 s93, s77, s93
	v_lshl_add_u64 v[250:251], s[92:93], 0, v[180:181]
	v_lshl_add_u64 v[252:253], s[92:93], 0, v[182:183]
	v_lshl_add_u64 v[222:223], s[92:93], 0, v[184:185]
	v_lshl_add_u64 v[246:247], s[92:93], 0, v[186:187]
	s_setprio 1
	s_waitcnt lgkmcnt(11)
	v_mfma_f32_16x16x32_bf16 v[160:163], v[164:167], v[210:213], v[160:163]
	v_mfma_f32_16x16x32_bf16 v[156:159], v[172:175], v[210:213], v[156:159]
	s_waitcnt lgkmcnt(10)
	v_mfma_f32_16x16x32_bf16 v[152:155], v[164:167], v[218:221], v[152:155]
	v_mfma_f32_16x16x32_bf16 v[148:151], v[172:175], v[218:221], v[148:151]
	s_waitcnt lgkmcnt(9)
	v_mfma_f32_16x16x32_bf16 v[136:139], v[164:167], v[228:231], v[136:139]
	v_mfma_f32_16x16x32_bf16 v[132:135], v[172:175], v[228:231], v[132:135]
	s_waitcnt lgkmcnt(8)
	v_mfma_f32_16x16x32_bf16 v[120:123], v[164:167], v[236:239], v[120:123]
	v_mfma_f32_16x16x32_bf16 v[116:119], v[172:175], v[236:239], v[116:119]
	ds_read_b64_tr_b16 v[164:165], v190 offset:16384
	ds_read_b64_tr_b16 v[166:167], v191 offset:16384
	ds_read_b64_tr_b16 v[172:173], v192 offset:16384
	ds_read_b64_tr_b16 v[174:175], v193 offset:16384
	s_waitcnt lgkmcnt(7)
	v_mfma_f32_16x16x32_bf16 v[160:163], v[168:171], v[214:217], v[160:163]
	v_mfma_f32_16x16x32_bf16 v[156:159], v[176:179], v[214:217], v[156:159]
	s_waitcnt lgkmcnt(6)
	v_mfma_f32_16x16x32_bf16 v[152:155], v[168:171], v[224:227], v[152:155]
	v_mfma_f32_16x16x32_bf16 v[148:151], v[176:179], v[224:227], v[148:151]
	s_waitcnt lgkmcnt(5)
	v_mfma_f32_16x16x32_bf16 v[136:139], v[168:171], v[232:235], v[136:139]
	v_mfma_f32_16x16x32_bf16 v[132:135], v[176:179], v[232:235], v[132:135]
	s_waitcnt lgkmcnt(4)
	v_mfma_f32_16x16x32_bf16 v[120:123], v[168:171], v[240:243], v[120:123]
	v_mfma_f32_16x16x32_bf16 v[116:119], v[176:179], v[240:243], v[116:119]
	ds_read_b64_tr_b16 v[168:169], v190 offset:24576
	ds_read_b64_tr_b16 v[170:171], v191 offset:24576
	ds_read_b64_tr_b16 v[176:177], v192 offset:24576
	ds_read_b64_tr_b16 v[178:179], v193 offset:24576
	s_waitcnt lgkmcnt(4)
	v_mfma_f32_16x16x32_bf16 v[144:147], v[164:167], v[210:213], v[144:147]
	v_mfma_f32_16x16x32_bf16 v[140:143], v[172:175], v[210:213], v[140:143]
	ds_read_b128 v[210:213], v207 offset:16384
	v_mfma_f32_16x16x32_bf16 v[128:131], v[164:167], v[218:221], v[128:131]
	v_mfma_f32_16x16x32_bf16 v[124:127], v[172:175], v[218:221], v[124:127]
	ds_read_b128 v[218:221], v207 offset:18432
	v_mfma_f32_16x16x32_bf16 v[112:115], v[164:167], v[228:231], v[112:115]
	v_mfma_f32_16x16x32_bf16 v[108:111], v[172:175], v[228:231], v[108:111]
	ds_read_b128 v[228:231], v207 offset:20480
	v_mfma_f32_16x16x32_bf16 v[104:107], v[164:167], v[236:239], v[104:107]
	v_mfma_f32_16x16x32_bf16 v[100:103], v[172:175], v[236:239], v[100:103]
	ds_read_b128 v[236:239], v207 offset:22528
	ds_read_b64_tr_b16 v[164:165], v190 offset:0
	ds_read_b64_tr_b16 v[166:167], v191 offset:0
	ds_read_b64_tr_b16 v[172:173], v192 offset:0
	ds_read_b64_tr_b16 v[174:175], v193 offset:0
	s_waitcnt lgkmcnt(8)
	v_mfma_f32_16x16x32_bf16 v[144:147], v[168:171], v[214:217], v[144:147]
	v_mfma_f32_16x16x32_bf16 v[140:143], v[176:179], v[214:217], v[140:143]
	ds_read_b128 v[214:217], v207 offset:17408
	v_mfma_f32_16x16x32_bf16 v[128:131], v[168:171], v[224:227], v[128:131]
	v_mfma_f32_16x16x32_bf16 v[124:127], v[176:179], v[224:227], v[124:127]
	ds_read_b128 v[224:227], v207 offset:19456
	v_mfma_f32_16x16x32_bf16 v[112:115], v[168:171], v[232:235], v[112:115]
	v_mfma_f32_16x16x32_bf16 v[108:111], v[176:179], v[232:235], v[108:111]
	ds_read_b128 v[232:235], v207 offset:21504
	v_mfma_f32_16x16x32_bf16 v[104:107], v[168:171], v[240:243], v[104:107]
	v_mfma_f32_16x16x32_bf16 v[100:103], v[176:179], v[240:243], v[100:103]
	ds_read_b128 v[240:243], v207 offset:23552
	ds_read_b64_tr_b16 v[168:169], v190 offset:8192
	ds_read_b64_tr_b16 v[170:171], v191 offset:8192
	ds_read_b64_tr_b16 v[176:177], v192 offset:8192
	ds_read_b64_tr_b16 v[178:179], v193 offset:8192
	s_waitcnt lgkmcnt(8)
	v_mfma_f32_16x16x32_bf16 v[80:83], v[164:167], v[210:213], v[80:83]
	v_mfma_f32_16x16x32_bf16 v[68:71], v[172:175], v[210:213], v[68:71]
	v_mfma_f32_16x16x32_bf16 v[48:51], v[164:167], v[218:221], v[48:51]
	v_mfma_f32_16x16x32_bf16 v[44:47], v[172:175], v[218:221], v[44:47]
	v_mfma_f32_16x16x32_bf16 v[32:35], v[164:167], v[228:231], v[32:35]
	v_mfma_f32_16x16x32_bf16 v[28:31], v[172:175], v[228:231], v[28:31]
	v_mfma_f32_16x16x32_bf16 v[16:19], v[164:167], v[236:239], v[16:19]
	v_mfma_f32_16x16x32_bf16 v[12:15], v[172:175], v[236:239], v[12:15]
	ds_read_b64_tr_b16 v[164:165], v190 offset:16384
	ds_read_b64_tr_b16 v[166:167], v191 offset:16384
	ds_read_b64_tr_b16 v[172:173], v192 offset:16384
	ds_read_b64_tr_b16 v[174:175], v193 offset:16384
	s_waitcnt lgkmcnt(4)
	v_mfma_f32_16x16x32_bf16 v[80:83], v[168:171], v[214:217], v[80:83]
	v_mfma_f32_16x16x32_bf16 v[68:71], v[176:179], v[214:217], v[68:71]
	v_mfma_f32_16x16x32_bf16 v[48:51], v[168:171], v[224:227], v[48:51]
	v_mfma_f32_16x16x32_bf16 v[44:47], v[176:179], v[224:227], v[44:47]
	v_mfma_f32_16x16x32_bf16 v[32:35], v[168:171], v[232:235], v[32:35]
	v_mfma_f32_16x16x32_bf16 v[28:31], v[176:179], v[232:235], v[28:31]
	v_mfma_f32_16x16x32_bf16 v[16:19], v[168:171], v[240:243], v[16:19]
	v_mfma_f32_16x16x32_bf16 v[12:15], v[176:179], v[240:243], v[12:15]
	ds_read_b64_tr_b16 v[168:169], v190 offset:24576
	ds_read_b64_tr_b16 v[170:171], v191 offset:24576
	ds_read_b64_tr_b16 v[176:177], v192 offset:24576
	ds_read_b64_tr_b16 v[178:179], v193 offset:24576
	s_waitcnt lgkmcnt(4)
	v_mfma_f32_16x16x32_bf16 v[56:59], v[164:167], v[210:213], v[56:59]
	v_mfma_f32_16x16x32_bf16 v[52:55], v[172:175], v[210:213], v[52:55]
	s_waitcnt vmcnt(11)
	v_cvt_pk_bf16_f32 v244, v64, v65
	v_cvt_pk_bf16_f32 v245, v66, v67
	ds_write_b64 v199, v[244:245]
	s_add_u32 s78, s50, 0x8000
	s_addc_u32 s79, s51, 0
	global_load_dwordx4 v[64:67], v189, s[78:79]
	v_mfma_f32_16x16x32_bf16 v[40:43], v[164:167], v[218:221], v[40:43]
	v_mfma_f32_16x16x32_bf16 v[36:39], v[172:175], v[218:221], v[36:39]
	s_waitcnt vmcnt(11)
	v_cvt_pk_bf16_f32 v244, v60, v61
	v_cvt_pk_bf16_f32 v245, v62, v63
	ds_write_b64 v200, v[244:245]
	s_add_u32 s80, s50, 0xc000
	s_addc_u32 s81, s51, 0
	global_load_dwordx4 v[60:63], v189, s[80:81]
	v_mfma_f32_16x16x32_bf16 v[24:27], v[164:167], v[228:231], v[24:27]
	v_mfma_f32_16x16x32_bf16 v[20:23], v[172:175], v[228:231], v[20:23]
	s_waitcnt vmcnt(11)
	v_cvt_pk_bf16_f32 v244, v76, v77
	v_cvt_pk_bf16_f32 v245, v78, v79
	ds_write_b64 v201, v[244:245]
	s_add_u32 s78, s50, 0x4000
	s_addc_u32 s79, s51, 0
	global_load_dwordx4 v[76:79], v189, s[78:79]
	v_mfma_f32_16x16x32_bf16 v[8:11], v[164:167], v[236:239], v[8:11]
	v_mfma_f32_16x16x32_bf16 v[2:5], v[172:175], v[236:239], v[4:7]
	s_waitcnt vmcnt(11)
	v_cvt_pk_bf16_f32 v244, v72, v73
	v_cvt_pk_bf16_f32 v245, v74, v75
	ds_write_b64 v202, v[244:245]
	s_add_u32 s80, s72, 0xc000
	s_addc_u32 s81, s73, 0
	global_load_dwordx4 v[72:75], v189, s[80:81]
	s_waitcnt lgkmcnt(4)
	v_mfma_f32_16x16x32_bf16 v[56:59], v[168:171], v[214:217], v[56:59]
	v_mfma_f32_16x16x32_bf16 v[52:55], v[176:179], v[214:217], v[52:55]
	s_waitcnt vmcnt(11)
	v_cvt_pk_bf16_f32 v244, v88, v89
	v_cvt_pk_bf16_f32 v245, v90, v91
	ds_write_b64 v203, v[244:245]
	global_load_dwordx4 v[88:91], v189, s[50:51]
	v_mfma_f32_16x16x32_bf16 v[40:43], v[168:171], v[224:227], v[40:43]
	v_mfma_f32_16x16x32_bf16 v[36:39], v[176:179], v[224:227], v[36:39]
	s_waitcnt vmcnt(11)
	v_cvt_pk_bf16_f32 v244, v84, v85
	v_cvt_pk_bf16_f32 v245, v86, v87
	ds_write_b64 v204, v[244:245]
	s_add_u32 s80, s72, 0x8000
	s_addc_u32 s81, s73, 0
	global_load_dwordx4 v[84:87], v189, s[80:81]
	v_mfma_f32_16x16x32_bf16 v[24:27], v[168:171], v[232:235], v[24:27]
	v_mfma_f32_16x16x32_bf16 v[20:23], v[176:179], v[232:235], v[20:23]
	s_waitcnt vmcnt(11)
	v_cvt_pk_bf16_f32 v244, v96, v97
	v_cvt_pk_bf16_f32 v245, v98, v99
	ds_write_b64 v205, v[244:245]
	global_load_dwordx4 v[96:99], v189, s[72:73]
	v_mfma_f32_16x16x32_bf16 v[8:11], v[168:171], v[240:243], v[8:11]
	v_mfma_f32_16x16x32_bf16 v[4:7], v[176:179], v[240:243], v[2:5]
	s_waitcnt vmcnt(11)
	v_cvt_pk_bf16_f32 v244, v92, v93
	v_cvt_pk_bf16_f32 v245, v94, v95
	ds_write_b64 v206, v[244:245]
	s_add_u32 s80, s72, 0x4000
	s_addc_u32 s81, s73, 0
	global_load_dwordx4 v[92:95], v189, s[80:81]
	s_setprio 0
.LBB0_862:
.Lswp_dnE_tail:
	s_lshl_b64 s[50:51], s[48:49], 7
	s_add_u32 s50, s82, s50
	s_addc_u32 s51, s77, s51
	s_mov_b32 m0, s21
	s_waitcnt vmcnt(8)
	s_waitcnt lgkmcnt(0)
	s_barrier
	global_load_lds_dwordx4 v[250:251], off
	s_mov_b32 m0, s67
	v_cndmask_b32_e32 v1, v209, v208, vcc
	global_load_lds_dwordx4 v[252:253], off
	v_cmp_ne_u32_e32 vcc, 0, v1
	s_mov_b64 s[96:97], vcc
	s_add_i32 m0, s21, 0x4000
	s_cbranch_vccnz .LBB0_864
	global_load_lds_dwordx4 v[222:223], off
	s_add_i32 m0, s21, 0x6000
	s_nop 0
	global_load_lds_dwordx4 v[246:247], off

.Lswp_dnE_half:
	ds_read_b64_tr_b16 v[164:165], v190 offset:0
	ds_read_b64_tr_b16 v[166:167], v191 offset:0
	ds_read_b64_tr_b16 v[172:173], v192 offset:0
	ds_read_b64_tr_b16 v[174:175], v193 offset:0
	ds_read_b128 v[210:213], v207
	ds_read_b128 v[218:221], v207 offset:2048
	ds_read_b128 v[228:231], v207 offset:4096
	ds_read_b128 v[236:239], v207 offset:6144
	ds_read_b64_tr_b16 v[168:169], v190 offset:8192
	ds_read_b64_tr_b16 v[170:171], v191 offset:8192
	ds_read_b64_tr_b16 v[176:177], v192 offset:8192
	ds_read_b64_tr_b16 v[178:179], v193 offset:8192
	ds_read_b128 v[214:217], v207 offset:1024
	ds_read_b128 v[224:227], v207 offset:3072
	ds_read_b128 v[232:235], v207 offset:5120
	ds_read_b128 v[240:243], v207 offset:7168
	s_add_i32 s48, s48, 2
	s_cmp_eq_u32 s35, 12
	s_cselect_b32 s48, 0, s48
	s_cselect_b32 s77, s41, s23
	s_cselect_b32 s82, s40, s22
	s_cselect_b32 s35, s39, s47
	s_cselect_b32 s37, s38, s46
	s_cselect_b32 s43, s27, s45
	s_cselect_b32 s74, s26, s44
	s_cselect_b64 vcc, -1, 0
	s_ashr_i32 s49, s48, 31
	s_lshl_b64 s[50:51], s[48:49], 19
	s_add_u32 s72, s74, s50
	s_addc_u32 s73, s43, s51
	s_add_u32 s50, s37, s50
	s_addc_u32 s51, s35, s51
	s_lshl_b64 s[92:93], s[48:49], 7
	s_add_u32 s92, s82, s92
	s_addc_u32 s93, s77, s93
	v_lshl_add_u64 v[250:251], s[92:93], 0, v[180:181]
	v_lshl_add_u64 v[252:253], s[92:93], 0, v[182:183]
	v_lshl_add_u64 v[222:223], s[92:93], 0, v[184:185]
	v_lshl_add_u64 v[246:247], s[92:93], 0, v[186:187]
	s_setprio 1
	s_waitcnt lgkmcnt(11)
	v_mfma_f32_16x16x32_bf16 v[160:163], v[164:167], v[210:213], v[160:163]
	v_mfma_f32_16x16x32_bf16 v[156:159], v[172:175], v[210:213], v[156:159]
	s_waitcnt lgkmcnt(10)
	v_mfma_f32_16x16x32_bf16 v[152:155], v[164:167], v[218:221], v[152:155]
	v_mfma_f32_16x16x32_bf16 v[148:151], v[172:175], v[218:221], v[148:151]
	s_waitcnt lgkmcnt(9)
	v_mfma_f32_16x16x32_bf16 v[136:139], v[164:167], v[228:231], v[136:139]
	v_mfma_f32_16x16x32_bf16 v[132:135], v[172:175], v[228:231], v[132:135]
	s_waitcnt lgkmcnt(8)
	v_mfma_f32_16x16x32_bf16 v[120:123], v[164:167], v[236:239], v[120:123]
	v_mfma_f32_16x16x32_bf16 v[116:119], v[172:175], v[236:239], v[116:119]
	ds_read_b64_tr_b16 v[164:165], v190 offset:16384
	ds_read_b64_tr_b16 v[166:167], v191 offset:16384
	ds_read_b64_tr_b16 v[172:173], v192 offset:16384
	ds_read_b64_tr_b16 v[174:175], v193 offset:16384
	s_waitcnt lgkmcnt(7)
	v_mfma_f32_16x16x32_bf16 v[160:163], v[168:171], v[214:217], v[160:163]
	v_mfma_f32_16x16x32_bf16 v[156:159], v[176:179], v[214:217], v[156:159]
	s_waitcnt lgkmcnt(6)
	v_mfma_f32_16x16x32_bf16 v[152:155], v[168:171], v[224:227], v[152:155]
	v_mfma_f32_16x16x32_bf16 v[148:151], v[176:179], v[224:227], v[148:151]
	s_waitcnt lgkmcnt(5)
	v_mfma_f32_16x16x32_bf16 v[136:139], v[168:171], v[232:235], v[136:139]
	v_mfma_f32_16x16x32_bf16 v[132:135], v[176:179], v[232:235], v[132:135]
	s_waitcnt lgkmcnt(4)
	v_mfma_f32_16x16x32_bf16 v[120:123], v[168:171], v[240:243], v[120:123]
	v_mfma_f32_16x16x32_bf16 v[116:119], v[176:179], v[240:243], v[116:119]
	ds_read_b64_tr_b16 v[168:169], v190 offset:24576
	ds_read_b64_tr_b16 v[170:171], v191 offset:24576
	ds_read_b64_tr_b16 v[176:177], v192 offset:24576
	ds_read_b64_tr_b16 v[178:179], v193 offset:24576
	s_waitcnt lgkmcnt(4)
	v_mfma_f32_16x16x32_bf16 v[144:147], v[164:167], v[210:213], v[144:147]
	v_mfma_f32_16x16x32_bf16 v[140:143], v[172:175], v[210:213], v[140:143]
	s_waitcnt vmcnt(9)
	v_cvt_pk_bf16_f32 v244, v64, v65
	v_cvt_pk_bf16_f32 v245, v66, v67
	ds_write_b64 v199, v[244:245]
	s_add_u32 s78, s50, 0x8000
	s_addc_u32 s79, s51, 0
	global_load_dwordx4 v[64:67], v189, s[78:79]
	v_mfma_f32_16x16x32_bf16 v[128:131], v[164:167], v[218:221], v[128:131]
	v_mfma_f32_16x16x32_bf16 v[124:127], v[172:175], v[218:221], v[124:127]
	s_waitcnt vmcnt(9)
	v_cvt_pk_bf16_f32 v244, v60, v61
	v_cvt_pk_bf16_f32 v245, v62, v63
	ds_write_b64 v200, v[244:245]
	s_add_u32 s80, s50, 0xc000
	s_addc_u32 s81, s51, 0
	global_load_dwordx4 v[60:63], v189, s[80:81]
	v_mfma_f32_16x16x32_bf16 v[112:115], v[164:167], v[228:231], v[112:115]
	v_mfma_f32_16x16x32_bf16 v[108:111], v[172:175], v[228:231], v[108:111]
	s_waitcnt vmcnt(9)
	v_cvt_pk_bf16_f32 v244, v76, v77
	v_cvt_pk_bf16_f32 v245, v78, v79
	ds_write_b64 v201, v[244:245]
	s_add_u32 s78, s50, 0x4000
	s_addc_u32 s79, s51, 0
	global_load_dwordx4 v[76:79], v189, s[78:79]
	v_mfma_f32_16x16x32_bf16 v[104:107], v[164:167], v[236:239], v[104:107]
	v_mfma_f32_16x16x32_bf16 v[100:103], v[172:175], v[236:239], v[100:103]
	s_waitcnt vmcnt(9)
	v_cvt_pk_bf16_f32 v244, v72, v73
	v_cvt_pk_bf16_f32 v245, v74, v75
	ds_write_b64 v202, v[244:245]
	s_add_u32 s80, s72, 0xc000
	s_addc_u32 s81, s73, 0
	global_load_dwordx4 v[72:75], v189, s[80:81]
	s_waitcnt lgkmcnt(4)
	v_mfma_f32_16x16x32_bf16 v[144:147], v[168:171], v[214:217], v[144:147]
	v_mfma_f32_16x16x32_bf16 v[140:143], v[176:179], v[214:217], v[140:143]
	s_waitcnt vmcnt(9)
	v_cvt_pk_bf16_f32 v244, v88, v89
	v_cvt_pk_bf16_f32 v245, v90, v91
	ds_write_b64 v203, v[244:245]
	global_load_dwordx4 v[88:91], v189, s[50:51]
	v_mfma_f32_16x16x32_bf16 v[128:131], v[168:171], v[224:227], v[128:131]
	v_mfma_f32_16x16x32_bf16 v[124:127], v[176:179], v[224:227], v[124:127]
	s_waitcnt vmcnt(9)
	v_cvt_pk_bf16_f32 v244, v84, v85
	v_cvt_pk_bf16_f32 v245, v86, v87
	ds_write_b64 v204, v[244:245]
	s_add_u32 s80, s72, 0x8000
	s_addc_u32 s81, s73, 0
	global_load_dwordx4 v[84:87], v189, s[80:81]
	v_mfma_f32_16x16x32_bf16 v[112:115], v[168:171], v[232:235], v[112:115]
	v_mfma_f32_16x16x32_bf16 v[108:111], v[176:179], v[232:235], v[108:111]
	s_waitcnt vmcnt(9)
	v_cvt_pk_bf16_f32 v244, v96, v97
	v_cvt_pk_bf16_f32 v245, v98, v99
	ds_write_b64 v205, v[244:245]
	global_load_dwordx4 v[96:99], v189, s[72:73]
	v_mfma_f32_16x16x32_bf16 v[104:107], v[168:171], v[240:243], v[104:107]
	v_mfma_f32_16x16x32_bf16 v[100:103], v[176:179], v[240:243], v[100:103]
	s_waitcnt vmcnt(9)
	v_cvt_pk_bf16_f32 v244, v92, v93
	v_cvt_pk_bf16_f32 v245, v94, v95
	ds_write_b64 v206, v[244:245]
	s_add_u32 s80, s72, 0x4000
	s_addc_u32 s81, s73, 0
	global_load_dwordx4 v[92:95], v189, s[80:81]
	s_setprio 0
	s_branch .Lswp_dnE_tail
